# v23 + weight-conversion output stores agent-scope write-through (sc1 instead of nt): no dirty converted weights left in L2 for the grid-barrier writeback
# baseline (speedup 1.0000x reference)
.LBB0_32:
	s_xor_b64 s[22:23], s[24:25], -1
	s_sub_i32 s8, s19, s9
	s_and_b64 s[24:25], s[24:25], exec
	s_cselect_b32 s21, s8, 0
	s_abs_i32 s24, s27
	v_cvt_f32_u32_e32 v2, s24
	s_sub_i32 s29, 0, s24
	s_abs_i32 s28, s21
	s_xor_b32 s25, s21, s27
	v_rcp_iflag_f32_e32 v2, v2
	s_ashr_i32 s25, s25, 31
	v_mov_b32_e32 v95, v83
	s_waitcnt vmcnt(5)
	v_cndmask_b32_e64 v78, v78, 1.0, s[4:5]
	v_mul_f32_e32 v2, 0x4f7ffffe, v2
	v_cvt_u32_f32_e32 v2, v2
	s_waitcnt vmcnt(4)
	v_cndmask_b32_e64 v74, v74, 1.0, s[4:5]
	s_waitcnt vmcnt(0)
	v_cmp_eq_u64_e32 vcc, 0, v[86:87]
	v_mov_b32_e32 v97, v83
	v_readfirstlane_b32 s30, v2
	s_mul_i32 s29, s29, s30
	s_mul_hi_u32 s29, s30, s29
	s_add_i32 s30, s30, s29
	s_mul_hi_u32 s29, s28, s30
	s_mul_i32 s30, s29, s24
	s_sub_i32 s28, s28, s30
	s_add_i32 s31, s29, 1
	s_sub_i32 s30, s28, s24
	s_cmp_ge_u32 s28, s24
	s_cselect_b32 s29, s31, s29
	s_cselect_b32 s28, s30, s28
	s_add_i32 s30, s29, 1
	s_cmp_ge_u32 s28, s24
	s_cselect_b32 s24, s30, s29
	s_xor_b32 s24, s24, s25
	s_sub_i32 s28, s24, s25
	s_lshl_b32 s24, s28, 6
	s_ashr_i32 s25, s24, 31
	v_lshl_add_u64 v[2:3], s[24:25], 2, v[86:87]
	s_mul_i32 s28, s28, s27
	v_lshl_add_u64 v[2:3], v[2:3], 0, v[94:95]
	v_cndmask_b32_e64 v95, v81, 1.0, s[4:5]
	v_cndmask_b32_e64 v94, v79, 1.0, s[4:5]
	v_cndmask_b32_e64 v79, v80, 1.0, s[4:5]
	v_cndmask_b32_e64 v81, v77, 1.0, s[4:5]
	v_cndmask_b32_e64 v80, v75, 1.0, s[4:5]
	v_cndmask_b32_e64 v75, v76, 1.0, s[4:5]
	s_sub_i32 s4, s21, s28
	s_lshl_b32 s4, s4, 5
	v_cndmask_b32_e32 v31, v3, v85, vcc
	v_cndmask_b32_e32 v30, v2, v84, vcc
	v_or_b32_e32 v32, s24, v1
	s_ashr_i32 s5, s4, 31
	global_load_dwordx4 v[2:5], v[30:31], off
	global_load_dwordx4 v[6:9], v[30:31], off offset:16
	s_mul_i32 s27, s20, s25
	v_mad_u64_u32 v[30:31], s[24:25], s20, v32, 0
	v_or_b32_e32 v33, 8, v32
	v_or_b32_e32 v34, 16, v32
	v_or_b32_e32 v36, 24, v32
	v_or_b32_e32 v38, 32, v32
	v_or_b32_e32 v40, 40, v32
	v_or_b32_e32 v42, 48, v32
	v_or_b32_e32 v44, 56, v32
	v_lshl_add_u64 v[46:47], s[4:5], 2, v[84:85]
	v_add_u32_e32 v31, s27, v31
	v_mad_u64_u32 v[32:33], s[24:25], s20, v33, 0
	v_mad_u64_u32 v[34:35], s[24:25], s20, v34, 0
	v_mad_u64_u32 v[36:37], s[24:25], s20, v36, 0
	v_mad_u64_u32 v[38:39], s[24:25], s20, v38, 0
	v_mad_u64_u32 v[40:41], s[24:25], s20, v40, 0
	v_mad_u64_u32 v[42:43], s[24:25], s20, v42, 0
	v_mad_u64_u32 v[44:45], s[20:21], s20, v44, 0
	v_lshl_add_u64 v[46:47], v[46:47], 0, v[82:83]
	ds_write2_b32 v101, v70, v71 offset1:1
	ds_write2_b32 v101, v72, v73 offset0:2 offset1:3
	ds_write2_b32 v112, v66, v67 offset1:1
	ds_write2_b32 v113, v68, v69 offset1:1
	ds_write2_b32 v114, v58, v59 offset1:1
	ds_write2_b32 v115, v60, v61 offset1:1
	v_add_u32_e32 v33, s27, v33
	v_add_u32_e32 v35, s27, v35
	v_add_u32_e32 v37, s27, v37
	v_add_u32_e32 v39, s27, v39
	v_add_u32_e32 v41, s27, v41
	v_add_u32_e32 v43, s27, v43
	v_add_u32_e32 v45, s27, v45
	v_lshl_add_u64 v[58:59], v[30:31], 2, v[46:47]
	v_lshl_add_u64 v[60:61], v[32:33], 2, v[46:47]
	v_lshl_add_u64 v[66:67], v[34:35], 2, v[46:47]
	v_lshl_add_u64 v[68:69], v[36:37], 2, v[46:47]
	v_lshl_add_u64 v[70:71], v[38:39], 2, v[46:47]
	v_lshl_add_u64 v[72:73], v[40:41], 2, v[46:47]
	v_lshl_add_u64 v[76:77], v[42:43], 2, v[46:47]
	v_lshl_add_u64 v[112:113], v[44:45], 2, v[46:47]
	global_load_dwordx4 v[62:65], v[58:59], off nt
	global_load_dwordx4 v[54:57], v[60:61], off nt
	global_load_dwordx4 v[50:53], v[66:67], off nt
	global_load_dwordx4 v[46:49], v[68:69], off nt
	global_load_dwordx4 v[42:45], v[70:71], off nt
	global_load_dwordx4 v[38:41], v[72:73], off nt
	global_load_dwordx4 v[34:37], v[76:77], off nt
	global_load_dwordx4 v[30:33], v[112:113], off nt
	ds_write2_b32 v102, v26, v27 offset1:1
	ds_write2_b32 v103, v28, v29 offset1:1
	ds_write2_b32 v104, v22, v23 offset1:1
	ds_write2_b32 v105, v24, v25 offset1:1
	ds_write2_b32 v106, v18, v19 offset1:1
	ds_write2_b32 v107, v20, v21 offset1:1
	ds_write2_b32 v108, v14, v15 offset1:1
	ds_write2_b32 v109, v16, v17 offset1:1
	ds_write2_b32 v110, v10, v11 offset1:1
	ds_write2_b32 v111, v12, v13 offset1:1
	s_waitcnt lgkmcnt(0)
	ds_read2_b32 v[14:15], v100 offset1:8
	ds_read2_b32 v[16:17], v100 offset0:66 offset1:74
	ds_read2_b32 v[20:21], v100 offset0:33 offset1:41
	ds_read2_b32 v[22:23], v100 offset0:99 offset1:107
	ds_read2_b32 v[24:25], v100 offset0:132 offset1:140
	ds_read2_b32 v[26:27], v100 offset0:198 offset1:206
	ds_read2_b32 v[28:29], v100 offset0:165 offset1:173
	ds_read2_b32 v[58:59], v100 offset0:231 offset1:239
	s_waitcnt lgkmcnt(7)
	v_mov_b32_e32 v10, v14
	s_waitcnt lgkmcnt(5)
	v_mov_b32_e32 v12, v20
	s_waitcnt lgkmcnt(4)
	v_mov_b32_e32 v13, v22
	s_waitcnt lgkmcnt(3)
	v_mov_b32_e32 v60, v24
	s_waitcnt lgkmcnt(2)
	v_mov_b32_e32 v61, v26
	s_waitcnt lgkmcnt(1)
	v_mov_b32_e32 v66, v28
	s_waitcnt lgkmcnt(0)
	v_mov_b32_e32 v67, v58
	v_mov_b32_e32 v11, v16
	v_pk_mul_f32 v[12:13], v[80:81], v[12:13]
	v_pk_mul_f32 v[60:61], v[78:79], v[60:61]
	v_pk_mul_f32 v[66:67], v[94:95], v[66:67]
	s_ashr_i32 s20, s17, 3
	v_pk_mul_f32 v[10:11], v[74:75], v[10:11]
	v_bfe_u32 v14, v67, 16, 1
	v_bfe_u32 v20, v13, 16, 1
	v_bfe_u32 v24, v60, 16, 1
	s_ashr_i32 s21, s20, 31
	v_bfe_u32 v16, v66, 16, 1
	v_bfe_u32 v22, v12, 16, 1
	v_add3_u32 v20, v13, v20, s1
	v_add3_u32 v13, v67, v14, s1
	v_bfe_u32 v14, v10, 16, 1
	v_add3_u32 v24, v60, v24, s1
	s_ashr_i32 s17, s16, 31
	s_and_b32 s4, s18, 0xe0
	v_lshl_add_u64 v[18:19], v[92:93], 0, v[96:97]
	v_add3_u32 v22, v12, v22, s1
	v_add3_u32 v12, v66, v16, s1
	v_bfe_u32 v16, v11, 16, 1
	v_bfe_u32 v26, v61, 16, 1
	v_add3_u32 v10, v10, v14, s1
	v_lshrrev_b32_e32 v14, 16, v24
	s_lshl_b64 s[20:21], s[20:21], 20
	v_add3_u32 v26, v61, v26, s1
	v_add3_u32 v11, v11, v16, s1
	v_and_or_b32 v12, v12, s3, v14
	v_or_b32_e32 v14, s4, v1
	s_lshl_b64 s[16:17], s[16:17], 15
	v_lshl_add_u64 v[18:19], v[18:19], 0, s[20:21]
	v_lshrrev_b32_e32 v10, 16, v10
	v_lshrrev_b32_e32 v11, 16, v11
	v_lshrrev_b32_e32 v16, 16, v26
	v_lshl_add_u64 v[18:19], v[18:19], 0, s[16:17]
	v_lshlrev_b32_e32 v60, 7, v14
	v_mov_b32_e32 v61, v83
	v_and_or_b32 v13, v13, s3, v16
	v_and_or_b32 v11, v20, s3, v11
	v_and_or_b32 v10, v22, s3, v10
	v_lshl_add_u64 v[60:61], v[18:19], 0, v[60:61]
	v_mov_b32_e32 v16, v15
	v_mov_b32_e32 v22, v21
	v_mov_b32_e32 v58, v29
	global_store_dwordx4 v[60:61], v[10:13], off sc1
	v_mov_b32_e32 v26, v25
	v_pk_mul_f32 v[14:15], v[78:79], v[26:27]
	v_pk_mul_f32 v[10:11], v[74:75], v[16:17]
	v_pk_mul_f32 v[12:13], v[80:81], v[22:23]
	v_pk_mul_f32 v[16:17], v[94:95], v[58:59]
	v_bfe_u32 v22, v13, 16, 1
	v_bfe_u32 v20, v17, 16, 1
	v_bfe_u32 v21, v16, 16, 1
	v_bfe_u32 v23, v12, 16, 1
	v_add3_u32 v22, v13, v22, s1
	v_add3_u32 v13, v17, v20, s1
	v_bfe_u32 v20, v14, 16, 1
	v_add3_u32 v23, v12, v23, s1
	v_add3_u32 v12, v16, v21, s1
	v_bfe_u32 v21, v15, 16, 1
	v_add3_u32 v14, v14, v20, s1
	v_bfe_u32 v16, v10, 16, 1
	v_bfe_u32 v17, v11, 16, 1
	v_add3_u32 v15, v15, v21, s1
	v_lshrrev_b32_e32 v14, 16, v14
	v_add3_u32 v11, v11, v17, s1
	v_add3_u32 v10, v10, v16, s1
	v_lshrrev_b32_e32 v15, 16, v15
	v_and_or_b32 v12, v12, s3, v14
	v_or_b32_e32 v14, s4, v89
	v_lshrrev_b32_e32 v10, 16, v10
	v_lshrrev_b32_e32 v11, 16, v11
	v_and_or_b32 v13, v13, s3, v15
	v_lshlrev_b32_e32 v14, 7, v14
	v_mov_b32_e32 v15, v83
	v_and_or_b32 v11, v22, s3, v11
	v_and_or_b32 v10, v23, s3, v10
	v_lshl_add_u64 v[14:15], v[18:19], 0, v[14:15]
	ds_read2_b32 v[16:17], v100 offset0:16 offset1:24
	ds_read2_b32 v[20:21], v100 offset0:82 offset1:90
	global_store_dwordx4 v[14:15], v[10:13], off sc1
	ds_read2_b32 v[14:15], v100 offset0:49 offset1:57
	ds_read2_b32 v[22:23], v100 offset0:115 offset1:123
	ds_read2_b32 v[24:25], v100 offset0:148 offset1:156
	ds_read2_b32 v[26:27], v100 offset0:214 offset1:222
	ds_read2_b32 v[28:29], v100 offset0:181 offset1:189
	ds_read2_b32 v[58:59], v100 offset0:247 offset1:255
	s_waitcnt lgkmcnt(7)
	v_mov_b32_e32 v10, v16
	s_waitcnt lgkmcnt(5)
	v_mov_b32_e32 v12, v14
	s_waitcnt lgkmcnt(4)
	v_mov_b32_e32 v13, v22
	s_waitcnt lgkmcnt(3)
	v_mov_b32_e32 v60, v24
	s_waitcnt lgkmcnt(2)
	v_mov_b32_e32 v61, v26
	s_waitcnt lgkmcnt(1)
	v_mov_b32_e32 v66, v28
	s_waitcnt lgkmcnt(0)
	v_mov_b32_e32 v67, v58
	v_mov_b32_e32 v11, v20
	v_pk_mul_f32 v[12:13], v[80:81], v[12:13]
	v_pk_mul_f32 v[60:61], v[78:79], v[60:61]
	v_pk_mul_f32 v[66:67], v[94:95], v[66:67]
	v_pk_mul_f32 v[10:11], v[74:75], v[10:11]
	v_bfe_u32 v14, v67, 16, 1
	v_bfe_u32 v20, v13, 16, 1
	v_bfe_u32 v24, v60, 16, 1
	v_bfe_u32 v16, v66, 16, 1
	v_bfe_u32 v22, v12, 16, 1
	v_add3_u32 v20, v13, v20, s1
	v_add3_u32 v13, v67, v14, s1
	v_bfe_u32 v14, v10, 16, 1
	v_add3_u32 v24, v60, v24, s1
	v_add3_u32 v22, v12, v22, s1
	v_add3_u32 v12, v66, v16, s1
	v_bfe_u32 v16, v11, 16, 1
	v_bfe_u32 v26, v61, 16, 1
	v_add3_u32 v10, v10, v14, s1
	v_lshrrev_b32_e32 v14, 16, v24
	v_add3_u32 v26, v61, v26, s1
	v_add3_u32 v11, v11, v16, s1
	v_and_or_b32 v12, v12, s3, v14
	v_or_b32_e32 v14, s4, v98
	v_lshrrev_b32_e32 v10, 16, v10
	v_lshrrev_b32_e32 v11, 16, v11
	v_lshrrev_b32_e32 v16, 16, v26
	v_lshlrev_b32_e32 v60, 7, v14
	v_mov_b32_e32 v61, v83
	v_and_or_b32 v13, v13, s3, v16
	v_and_or_b32 v11, v20, s3, v11
	v_and_or_b32 v10, v22, s3, v10
	v_lshl_add_u64 v[60:61], v[18:19], 0, v[60:61]
	v_mov_b32_e32 v22, v15
	v_mov_b32_e32 v58, v29
	global_store_dwordx4 v[60:61], v[10:13], off sc1
	v_mov_b32_e32 v20, v17
	v_mov_b32_e32 v26, v25
	v_pk_mul_f32 v[12:13], v[80:81], v[22:23]
	v_pk_mul_f32 v[16:17], v[94:95], v[58:59]
	v_pk_mul_f32 v[10:11], v[74:75], v[20:21]
	v_pk_mul_f32 v[14:15], v[78:79], v[26:27]
	v_bfe_u32 v20, v17, 16, 1
	v_bfe_u32 v22, v13, 16, 1
	v_bfe_u32 v21, v16, 16, 1
	v_bfe_u32 v23, v12, 16, 1
	v_add3_u32 v22, v13, v22, s1
	v_add3_u32 v13, v17, v20, s1
	v_bfe_u32 v20, v14, 16, 1
	v_add3_u32 v23, v12, v23, s1
	v_add3_u32 v12, v16, v21, s1
	v_bfe_u32 v21, v15, 16, 1
	v_add3_u32 v14, v14, v20, s1
	v_bfe_u32 v16, v10, 16, 1
	v_bfe_u32 v17, v11, 16, 1
	v_add3_u32 v15, v15, v21, s1
	v_lshrrev_b32_e32 v14, 16, v14
	v_add3_u32 v11, v11, v17, s1
	v_add3_u32 v10, v10, v16, s1
	v_lshrrev_b32_e32 v15, 16, v15
	v_and_or_b32 v12, v12, s3, v14
	v_or_b32_e32 v14, s4, v99
	v_lshrrev_b32_e32 v10, 16, v10
	v_lshrrev_b32_e32 v11, 16, v11
	v_and_or_b32 v13, v13, s3, v15
	v_lshlrev_b32_e32 v14, 7, v14
	v_mov_b32_e32 v15, v83
	v_and_or_b32 v11, v22, s3, v11
	v_and_or_b32 v10, v23, s3, v10
	v_lshl_add_u64 v[14:15], v[18:19], 0, v[14:15]
	global_store_dwordx4 v[14:15], v[10:13], off sc1
	s_waitcnt lgkmcnt(0)
	s_waitcnt vmcnt(13)
	v_cndmask_b32_e64 v5, v5, 1.0, vcc
	v_cndmask_b32_e64 v4, v4, 1.0, vcc
	v_cndmask_b32_e64 v3, v3, 1.0, vcc
	v_cndmask_b32_e64 v2, v2, 1.0, vcc
	s_waitcnt vmcnt(12)
	v_cndmask_b32_e64 v9, v9, 1.0, vcc
	v_cndmask_b32_e64 v8, v8, 1.0, vcc
	v_cndmask_b32_e64 v7, v7, 1.0, vcc
	v_cndmask_b32_e64 v6, v6, 1.0, vcc

.LBB0_47:
	s_sub_i32 s16, s21, s9
	s_and_b64 s[4:5], s[22:23], exec
	s_cselect_b32 s5, s16, 0
	s_lshr_b32 s27, s20, 5
	s_waitcnt vmcnt(6)
	v_cvt_f32_u32_e32 v10, s27
	s_sub_i32 s17, 0, s27
	s_abs_i32 s16, s5
	s_ashr_i32 s4, s5, 31
	v_rcp_iflag_f32_e32 v10, v10
	s_waitcnt vmcnt(7)
	ds_write2_b32 v101, v62, v63 offset1:1
	ds_write2_b32 v101, v64, v65 offset0:2 offset1:3
	v_add_u32_e32 v112, 0x420, v101
	s_waitcnt vmcnt(6)
	ds_write2_b32 v112, v54, v55 offset1:1
	v_mul_f32_e32 v10, 0x4f7ffffe, v10
	v_cvt_u32_f32_e32 v10, v10
	v_add_u32_e32 v114, 0x840, v101
	s_waitcnt vmcnt(5)
	ds_write2_b32 v114, v50, v51 offset1:1
	v_add_u32_e32 v102, 0xc60, v101
	v_readfirstlane_b32 s18, v10
	s_mul_i32 s17, s17, s18
	s_mul_hi_u32 s17, s18, s17
	s_add_i32 s18, s18, s17
	s_mul_hi_u32 s17, s16, s18
	s_mul_i32 s18, s17, s27
	s_sub_i32 s16, s16, s18
	s_add_i32 s19, s17, 1
	s_sub_i32 s18, s16, s27
	s_cmp_ge_u32 s16, s27
	s_cselect_b32 s17, s19, s17
	s_cselect_b32 s16, s18, s16
	s_add_i32 s18, s17, 1
	s_cmp_ge_u32 s16, s27
	s_cselect_b32 s16, s18, s17
	s_xor_b32 s16, s16, s4
	s_sub_i32 s16, s16, s4
	s_mul_i32 s17, s16, s27
	s_sub_i32 s17, s5, s17
	s_lshl_b32 s4, s16, 6
	s_lshl_b32 s18, s17, 5
	v_or_b32_e32 v14, s4, v1
	s_ashr_i32 s5, s4, 31
	s_ashr_i32 s19, s18, 31
	s_waitcnt vmcnt(0)
	v_lshl_add_u64 v[10:11], s[18:19], 2, v[84:85]
	s_mul_i32 s19, s5, s20
	v_mad_u64_u32 v[12:13], s[24:25], v14, s20, 0
	v_lshl_add_u64 v[10:11], v[10:11], 0, v[82:83]
	v_add_u32_e32 v13, s19, v13
	v_lshl_add_u64 v[62:63], v[12:13], 2, v[10:11]
	v_or_b32_e32 v12, 8, v14
	v_mad_u64_u32 v[12:13], s[24:25], v12, s20, 0
	v_add_u32_e32 v13, s19, v13
	v_lshl_add_u64 v[54:55], v[12:13], 2, v[10:11]
	v_or_b32_e32 v12, 16, v14
	v_mad_u64_u32 v[12:13], s[24:25], v12, s20, 0
	v_add_u32_e32 v13, s19, v13
	v_lshl_add_u64 v[50:51], v[12:13], 2, v[10:11]
	v_or_b32_e32 v12, 24, v14
	v_mad_u64_u32 v[12:13], s[24:25], v12, s20, 0
	v_add_u32_e32 v13, s19, v13
	ds_write2_b32 v102, v46, v47 offset1:1
	v_lshl_add_u64 v[46:47], v[12:13], 2, v[10:11]
	v_or_b32_e32 v12, 32, v14
	v_mad_u64_u32 v[12:13], s[24:25], v12, s20, 0
	v_add_u32_e32 v104, 0x1080, v101
	v_add_u32_e32 v13, s19, v13
	ds_write2_b32 v104, v42, v43 offset1:1
	v_lshl_add_u64 v[42:43], v[12:13], 2, v[10:11]
	v_or_b32_e32 v12, 40, v14
	v_mad_u64_u32 v[12:13], s[24:25], v12, s20, 0
	v_add_u32_e32 v106, 0x14a0, v101
	v_add_u32_e32 v13, s19, v13
	ds_write2_b32 v106, v38, v39 offset1:1
	v_lshl_add_u64 v[38:39], v[12:13], 2, v[10:11]
	v_or_b32_e32 v12, 48, v14
	v_mad_u64_u32 v[12:13], s[24:25], v12, s20, 0
	v_add_u32_e32 v107, 0x14a8, v101
	v_add_u32_e32 v13, s19, v13
	ds_write2_b32 v107, v40, v41 offset1:1
	v_lshl_add_u64 v[40:41], v[12:13], 2, v[10:11]
	v_or_b32_e32 v12, 56, v14
	v_mad_u64_u32 v[12:13], s[24:25], v12, s20, 0
	v_add_u32_e32 v105, 0x1088, v101
	v_add_u32_e32 v13, s19, v13
	v_add_u32_e32 v113, 0x428, v101
	v_add_u32_e32 v115, 0x848, v101
	v_add_u32_e32 v103, 0xc68, v101
	ds_write2_b32 v105, v44, v45 offset1:1
	v_lshl_add_u64 v[44:45], v[12:13], 2, v[10:11]
	v_add_u32_e32 v108, 0x18c0, v101
	v_add_u32_e32 v109, 0x18c8, v101
	v_lshl_add_u64 v[10:11], s[4:5], 2, v[86:87]
	v_add_u32_e32 v110, 0x1ce0, v101
	v_add_u32_e32 v111, 0x1ce8, v101
	v_lshlrev_b32_e32 v94, 2, v88
	v_mov_b32_e32 v95, v83
	ds_write2_b32 v113, v56, v57 offset1:1
	ds_write2_b32 v115, v52, v53 offset1:1
	ds_write2_b32 v103, v48, v49 offset1:1
	ds_write2_b32 v108, v34, v35 offset1:1
	ds_write2_b32 v109, v36, v37 offset1:1
	ds_write2_b32 v110, v30, v31 offset1:1
	ds_write2_b32 v111, v32, v33 offset1:1
	v_lshl_add_u64 v[10:11], v[10:11], 0, v[94:95]
	v_cmp_eq_u64_e64 s[4:5], 0, v[86:87]
	s_lshr_b32 s19, s26, 5
	v_cvt_f32_u32_e32 v37, s19
	v_cndmask_b32_e64 v31, v11, v85, s[4:5]
	v_cndmask_b32_e64 v30, v10, v84, s[4:5]
	global_load_dwordx4 v[70:73], v[62:63], off nt
	global_load_dwordx4 v[66:69], v[54:55], off nt
	global_load_dwordx4 v[58:61], v[50:51], off nt
	global_load_dwordx4 v[26:29], v[46:47], off nt
	global_load_dwordx4 v[22:25], v[42:43], off nt
	global_load_dwordx4 v[18:21], v[38:39], off nt
	global_load_dwordx4 v[14:17], v[40:41], off nt
	global_load_dwordx4 v[10:13], v[44:45], off nt
	global_load_dwordx4 v[78:81], v[30:31], off offset:16
	global_load_dwordx4 v[74:77], v[30:31], off
	s_waitcnt lgkmcnt(0)
	ds_read2_b32 v[38:39], v100 offset0:33 offset1:41
	ds_read2_b32 v[40:41], v100 offset0:99 offset1:107
	ds_read2_b32 v[42:43], v100 offset0:165 offset1:173
	ds_read2_b32 v[44:45], v100 offset0:231 offset1:239
	v_mov_b32_e32 v31, v4
	v_mov_b32_e32 v4, v3
	s_waitcnt lgkmcnt(3)
	v_mov_b32_e32 v32, v38
	s_waitcnt lgkmcnt(2)
	v_mov_b32_e32 v33, v40
	v_pk_mul_f32 v[32:33], v[4:5], v[32:33]
	ds_read2_b32 v[46:47], v100 offset0:132 offset1:140
	ds_read2_b32 v[48:49], v100 offset0:198 offset1:206
	v_bfe_u32 v3, v32, 16, 1
	v_add3_u32 v38, v32, v3, s1
	v_bfe_u32 v3, v33, 16, 1
	v_add3_u32 v40, v33, v3, s1
	v_mov_b32_e32 v33, v8
	v_mov_b32_e32 v8, v7
	s_waitcnt lgkmcnt(3)
	v_mov_b32_e32 v34, v42
	s_waitcnt lgkmcnt(2)
	v_mov_b32_e32 v35, v44
	v_pk_mul_f32 v[34:35], v[8:9], v[34:35]
	ds_read2_b32 v[50:51], v100 offset1:8
	ds_read2_b32 v[52:53], v100 offset0:66 offset1:74
	v_bfe_u32 v3, v34, 16, 1
	v_mov_b32_e32 v32, v6
	s_waitcnt lgkmcnt(3)
	v_mov_b32_e32 v6, v46
	s_waitcnt lgkmcnt(2)
	v_mov_b32_e32 v7, v48
	v_add3_u32 v34, v34, v3, s1
	v_bfe_u32 v3, v35, 16, 1
	v_pk_mul_f32 v[6:7], v[32:33], v[6:7]
	v_add3_u32 v35, v35, v3, s1
	v_bfe_u32 v3, v7, 16, 1
	v_add3_u32 v7, v7, v3, s1
	v_bfe_u32 v3, v6, 16, 1
	v_add3_u32 v6, v6, v3, s1
	v_mov_b32_e32 v30, v2
	s_waitcnt lgkmcnt(1)
	v_mov_b32_e32 v2, v50
	s_waitcnt lgkmcnt(0)
	v_mov_b32_e32 v3, v52
	v_rcp_iflag_f32_e32 v42, v37
	v_pk_mul_f32 v[2:3], v[30:31], v[2:3]
	v_lshrrev_b32_e32 v6, 16, v6
	v_bfe_u32 v36, v3, 16, 1
	v_add3_u32 v3, v3, v36, s1
	v_bfe_u32 v36, v2, 16, 1
	v_add3_u32 v2, v2, v36, s1
	v_and_or_b32 v36, v34, s3, v6
	v_mul_f32_e32 v6, 0x4f7ffffe, v42
	v_cvt_u32_f32_e32 v6, v6
	s_sub_i32 s28, 0, s19
	s_abs_i32 s26, s8
	s_ashr_i32 s25, s8, 31
	v_readfirstlane_b32 s24, v6
	s_mul_i32 s28, s28, s24
	s_mul_hi_u32 s28, s24, s28
	s_add_i32 s24, s24, s28
	s_mul_hi_u32 s24, s26, s24
	s_mul_i32 s28, s24, s19
	s_sub_i32 s26, s26, s28
	s_add_i32 s28, s24, 1
	s_sub_i32 s29, s26, s19
	s_cmp_ge_u32 s26, s19
	s_cselect_b32 s24, s28, s24
	s_cselect_b32 s26, s29, s26
	s_add_i32 s28, s24, 1
	s_cmp_ge_u32 s26, s19
	s_cselect_b32 s24, s28, s24
	s_xor_b32 s24, s24, s25
	s_sub_i32 s24, s24, s25
	s_mul_i32 s19, s24, s19
	s_sub_i32 s8, s8, s19
	s_ashr_i32 s28, s8, 3
	v_lshrrev_b32_e32 v7, 16, v7
	v_lshrrev_b32_e32 v3, 16, v3
	v_lshrrev_b32_e32 v2, 16, v2
	s_ashr_i32 s29, s28, 31
	v_lshlrev_b32_e32 v96, 1, v88
	v_mov_b32_e32 v97, v83
	v_and_or_b32 v37, v35, s3, v7
	v_and_or_b32 v35, v40, s3, v3
	v_and_or_b32 v34, v38, s3, v2
	s_lshl_b32 s19, s8, 5
	s_ashr_i32 s25, s24, 31
	v_lshl_add_u64 v[2:3], v[90:91], 0, v[96:97]
	s_lshl_b64 s[28:29], s[28:29], 20
	s_and_b32 s8, s19, 0xe0
	s_lshl_b64 s[24:25], s[24:25], 15
	v_lshl_add_u64 v[2:3], v[2:3], 0, s[28:29]
	v_lshl_add_u64 v[6:7], v[2:3], 0, s[24:25]
	v_or_b32_e32 v2, s8, v1
	v_lshlrev_b32_e32 v2, 7, v2
	v_mov_b32_e32 v3, v83
	v_lshl_add_u64 v[2:3], v[6:7], 0, v[2:3]
	v_mov_b32_e32 v40, v39
	global_store_dwordx4 v[2:3], v[34:37], off sc1
	v_pk_mul_f32 v[2:3], v[4:5], v[40:41]
	v_mov_b32_e32 v44, v43
	v_bfe_u32 v34, v2, 16, 1
	v_add3_u32 v34, v2, v34, s1
	v_bfe_u32 v2, v3, 16, 1
	v_add3_u32 v35, v3, v2, s1
	v_pk_mul_f32 v[2:3], v[8:9], v[44:45]
	v_mov_b32_e32 v48, v47
	v_bfe_u32 v36, v2, 16, 1
	v_add3_u32 v36, v2, v36, s1
	v_bfe_u32 v2, v3, 16, 1
	v_add3_u32 v37, v3, v2, s1
	v_pk_mul_f32 v[2:3], v[32:33], v[48:49]
	v_mov_b32_e32 v52, v51
	v_bfe_u32 v38, v3, 16, 1
	v_add3_u32 v38, v3, v38, s1
	v_bfe_u32 v3, v2, 16, 1
	v_add3_u32 v39, v2, v3, s1
	v_pk_mul_f32 v[2:3], v[30:31], v[52:53]
	v_lshrrev_b32_e32 v39, 16, v39
	v_bfe_u32 v40, v3, 16, 1
	v_add3_u32 v3, v3, v40, s1
	v_bfe_u32 v40, v2, 16, 1
	v_add3_u32 v2, v2, v40, s1
	v_lshrrev_b32_e32 v38, 16, v38
	v_lshrrev_b32_e32 v2, 16, v2
	v_and_or_b32 v37, v37, s3, v38
	v_and_or_b32 v36, v36, s3, v39
	v_lshrrev_b32_e32 v3, 16, v3
	v_and_or_b32 v34, v34, s3, v2
	v_or_b32_e32 v2, s8, v89
	ds_read2_b32 v[38:39], v100 offset0:49 offset1:57
	ds_read2_b32 v[40:41], v100 offset0:115 offset1:123
	v_and_or_b32 v35, v35, s3, v3
	v_lshlrev_b32_e32 v2, 7, v2
	v_mov_b32_e32 v3, v83
	v_lshl_add_u64 v[2:3], v[6:7], 0, v[2:3]
	global_store_dwordx4 v[2:3], v[34:37], off sc1
	ds_read2_b32 v[42:43], v100 offset0:181 offset1:189
	ds_read2_b32 v[44:45], v100 offset0:247 offset1:255
	s_waitcnt lgkmcnt(3)
	v_mov_b32_e32 v2, v38
	s_waitcnt lgkmcnt(2)
	v_mov_b32_e32 v3, v40
	v_pk_mul_f32 v[2:3], v[4:5], v[2:3]
	ds_read2_b32 v[46:47], v100 offset0:148 offset1:156
	ds_read2_b32 v[48:49], v100 offset0:214 offset1:222
	v_bfe_u32 v34, v2, 16, 1
	v_add3_u32 v34, v2, v34, s1
	v_bfe_u32 v2, v3, 16, 1
	v_add3_u32 v35, v3, v2, s1
	s_waitcnt lgkmcnt(3)
	v_mov_b32_e32 v2, v42
	s_waitcnt lgkmcnt(2)
	v_mov_b32_e32 v3, v44
	v_pk_mul_f32 v[2:3], v[8:9], v[2:3]
	ds_read2_b32 v[50:51], v100 offset0:16 offset1:24
	ds_read2_b32 v[52:53], v100 offset0:82 offset1:90
	v_bfe_u32 v36, v2, 16, 1
	v_add3_u32 v36, v2, v36, s1
	v_bfe_u32 v2, v3, 16, 1
	v_add3_u32 v37, v3, v2, s1
	s_waitcnt lgkmcnt(3)
	v_mov_b32_e32 v2, v46
	s_waitcnt lgkmcnt(2)
	v_mov_b32_e32 v3, v48
	v_pk_mul_f32 v[2:3], v[32:33], v[2:3]
	v_mov_b32_e32 v44, v43
	v_bfe_u32 v38, v3, 16, 1
	v_add3_u32 v38, v3, v38, s1
	v_bfe_u32 v3, v2, 16, 1
	v_add3_u32 v40, v2, v3, s1
	s_waitcnt lgkmcnt(1)
	v_mov_b32_e32 v2, v50
	s_waitcnt lgkmcnt(0)
	v_mov_b32_e32 v3, v52
	v_pk_mul_f32 v[2:3], v[30:31], v[2:3]
	v_lshrrev_b32_e32 v40, 16, v40
	v_bfe_u32 v42, v3, 16, 1
	v_add3_u32 v3, v3, v42, s1
	v_bfe_u32 v42, v2, 16, 1
	v_add3_u32 v2, v2, v42, s1
	v_lshrrev_b32_e32 v2, 16, v2
	v_lshrrev_b32_e32 v3, 16, v3
	v_and_or_b32 v34, v34, s3, v2
	v_or_b32_e32 v2, s8, v98
	v_lshrrev_b32_e32 v38, 16, v38
	v_and_or_b32 v35, v35, s3, v3
	v_lshlrev_b32_e32 v2, 7, v2
	v_mov_b32_e32 v3, v83
	v_and_or_b32 v37, v37, s3, v38
	v_and_or_b32 v36, v36, s3, v40
	v_lshl_add_u64 v[2:3], v[6:7], 0, v[2:3]
	v_mov_b32_e32 v40, v39
	global_store_dwordx4 v[2:3], v[34:37], off sc1
	v_pk_mul_f32 v[2:3], v[4:5], v[40:41]
	v_mov_b32_e32 v52, v51
	v_mov_b32_e32 v48, v47
	v_pk_mul_f32 v[4:5], v[8:9], v[44:45]
	v_pk_mul_f32 v[8:9], v[30:31], v[52:53]
	v_pk_mul_f32 v[30:31], v[32:33], v[48:49]
	v_bfe_u32 v32, v2, 16, 1
	v_add3_u32 v2, v2, v32, s1
	v_bfe_u32 v32, v3, 16, 1
	v_add3_u32 v3, v3, v32, s1
	v_bfe_u32 v32, v4, 16, 1
	v_add3_u32 v4, v4, v32, s1
	v_bfe_u32 v32, v5, 16, 1
	v_add3_u32 v5, v5, v32, s1
	v_bfe_u32 v32, v31, 16, 1
	v_add3_u32 v31, v31, v32, s1
	v_bfe_u32 v32, v30, 16, 1
	v_add3_u32 v30, v30, v32, s1
	v_bfe_u32 v32, v9, 16, 1
	v_add3_u32 v9, v9, v32, s1
	v_bfe_u32 v32, v8, 16, 1
	v_add3_u32 v8, v8, v32, s1
	v_lshrrev_b32_e32 v8, 16, v8
	v_lshrrev_b32_e32 v9, 16, v9
	v_and_or_b32 v2, v2, s3, v8
	v_or_b32_e32 v8, s8, v99
	v_lshrrev_b32_e32 v30, 16, v30
	v_lshrrev_b32_e32 v31, 16, v31
	v_and_or_b32 v3, v3, s3, v9
	v_lshlrev_b32_e32 v8, 7, v8
	v_mov_b32_e32 v9, v83
	v_and_or_b32 v5, v5, s3, v31
	v_and_or_b32 v4, v4, s3, v30
	v_lshl_add_u64 v[6:7], v[6:7], 0, v[8:9]
	global_store_dwordx4 v[6:7], v[2:5], off sc1
	s_waitcnt lgkmcnt(0)
	s_andn2_b64 vcc, exec, s[22:23]
	s_mov_b64 s[22:23], -1
	s_cbranch_vccnz .LBB0_33
	s_add_i32 s19, s21, s0
	s_add_i32 s28, s9, s14
	s_cmp_lt_i32 s19, s28
	s_mov_b64 s[24:25], -1
	s_cbranch_scc1 .LBB0_31
	s_add_i32 s23, s15, 1
	s_max_i32 s22, s23, 1
	s_cmp_gt_i32 s15, -1
	s_mov_b64 s[24:25], 0
	s_cbranch_scc0 .LBB0_52
	s_mov_b32 s15, s22
	v_mov_b64_e32 v[90:91], v[92:93]
	s_mov_b64 s[8:9], s[20:21]
	s_branch .LBB0_59

.LBB0_843:
	s_xor_b64 s[8:9], s[28:29], -1
	s_sub_i32 s43, s50, s40
	s_and_b64 s[28:29], s[28:29], exec
	s_cselect_b32 s11, s43, 0
	s_abs_i32 s16, s41
	v_cvt_f32_u32_e32 v2, s16
	s_sub_i32 s29, 0, s16
	s_abs_i32 s28, s11
	s_xor_b32 s17, s11, s41
	v_rcp_iflag_f32_e32 v2, v2
	s_ashr_i32 s17, s17, 31
	v_mov_b32_e32 v97, v115
	s_waitcnt vmcnt(0)
	v_cmp_eq_u64_e32 vcc, 0, v[88:89]
	v_mul_f32_e32 v2, 0x4f7ffffe, v2
	v_cvt_u32_f32_e32 v2, v2
	v_cndmask_b32_e64 v78, v78, 1.0, s[38:39]
	v_cndmask_b32_e64 v74, v74, 1.0, s[38:39]
	v_mov_b32_e32 v95, v115
	v_readfirstlane_b32 s54, v2
	s_mul_i32 s29, s29, s54
	s_mul_hi_u32 s29, s54, s29
	s_add_i32 s54, s54, s29
	s_mul_hi_u32 s29, s28, s54
	s_mul_i32 s54, s29, s16
	s_sub_i32 s28, s28, s54
	s_add_i32 s56, s29, 1
	s_sub_i32 s54, s28, s16
	s_cmp_ge_u32 s28, s16
	s_cselect_b32 s29, s56, s29
	s_cselect_b32 s28, s54, s28
	s_add_i32 s54, s29, 1
	s_cmp_ge_u32 s28, s16
	s_cselect_b32 s16, s54, s29
	s_xor_b32 s16, s16, s17
	s_sub_i32 s16, s16, s17
	s_lshl_b32 s28, s16, 6
	s_mul_i32 s16, s16, s41
	s_ashr_i32 s29, s28, 31
	s_sub_i32 s11, s11, s16
	v_lshl_add_u64 v[2:3], s[28:29], 2, v[88:89]
	v_or_b32_e32 v12, s28, v87
	s_lshl_b32 s28, s11, 5
	s_mul_i32 s11, s55, s29
	v_or_b32_e32 v13, 8, v12
	v_or_b32_e32 v14, 16, v12
	v_or_b32_e32 v16, 24, v12
	v_or_b32_e32 v18, 32, v12
	v_or_b32_e32 v20, 40, v12
	v_or_b32_e32 v22, 48, v12
	v_or_b32_e32 v24, 56, v12
	s_ashr_i32 s29, s28, 31
	v_lshl_add_u64 v[2:3], v[2:3], 0, v[96:97]
	v_cndmask_b32_e64 v97, v81, 1.0, s[38:39]
	v_cndmask_b32_e64 v96, v79, 1.0, s[38:39]
	v_cndmask_b32_e64 v79, v80, 1.0, s[38:39]
	v_cndmask_b32_e64 v81, v77, 1.0, s[38:39]
	v_cndmask_b32_e64 v80, v75, 1.0, s[38:39]
	v_cndmask_b32_e64 v75, v76, 1.0, s[38:39]
	v_mad_u64_u32 v[10:11], s[38:39], s55, v12, 0
	v_mad_u64_u32 v[12:13], s[38:39], s55, v13, 0
	v_mad_u64_u32 v[14:15], s[38:39], s55, v14, 0
	v_mad_u64_u32 v[16:17], s[38:39], s55, v16, 0
	v_mad_u64_u32 v[18:19], s[38:39], s55, v18, 0
	v_mad_u64_u32 v[20:21], s[38:39], s55, v20, 0
	v_mad_u64_u32 v[22:23], s[38:39], s55, v22, 0
	v_mad_u64_u32 v[24:25], s[38:39], s55, v24, 0
	v_lshl_add_u64 v[26:27], s[28:29], 2, v[82:83]
	v_cndmask_b32_e32 v7, v3, v83, vcc
	v_cndmask_b32_e32 v6, v2, v82, vcc
	v_add_u32_e32 v11, s11, v11
	v_add_u32_e32 v13, s11, v13
	v_add_u32_e32 v15, s11, v15
	v_add_u32_e32 v17, s11, v17
	v_add_u32_e32 v19, s11, v19
	v_add_u32_e32 v21, s11, v21
	v_add_u32_e32 v23, s11, v23
	v_add_u32_e32 v25, s11, v25
	v_lshl_add_u64 v[26:27], v[26:27], 0, v[114:115]
	global_load_dwordx4 v[2:5], v[6:7], off
	s_nop 0
	global_load_dwordx4 v[6:9], v[6:7], off offset:16
	ds_write2_b32 v102, v66, v67 offset1:1
	ds_write2_b32 v102, v68, v69 offset0:2 offset1:3
	ds_write2_b32 v113, v62, v63 offset1:1
	ds_write2_b32 v116, v64, v65 offset1:1
	ds_write2_b32 v117, v70, v71 offset1:1
	ds_write2_b32 v118, v72, v73 offset1:1
	v_lshl_add_u64 v[10:11], v[10:11], 2, v[26:27]
	v_lshl_add_u64 v[28:29], v[12:13], 2, v[26:27]
	v_lshl_add_u64 v[30:31], v[14:15], 2, v[26:27]
	v_lshl_add_u64 v[32:33], v[16:17], 2, v[26:27]
	v_lshl_add_u64 v[34:35], v[18:19], 2, v[26:27]
	v_lshl_add_u64 v[36:37], v[20:21], 2, v[26:27]
	v_lshl_add_u64 v[38:39], v[22:23], 2, v[26:27]
	v_lshl_add_u64 v[40:41], v[24:25], 2, v[26:27]
	global_load_dwordx4 v[10:13], v[10:11], off nt
	s_nop 0
	global_load_dwordx4 v[14:17], v[28:29], off nt
	global_load_dwordx4 v[18:21], v[30:31], off nt
	global_load_dwordx4 v[22:25], v[32:33], off nt
	s_nop 0
	global_load_dwordx4 v[26:29], v[34:35], off nt
	global_load_dwordx4 v[30:33], v[36:37], off nt
	s_nop 0
	global_load_dwordx4 v[34:37], v[38:39], off nt
	s_nop 0
	global_load_dwordx4 v[38:41], v[40:41], off nt
	ds_write2_b32 v103, v42, v43 offset1:1
	ds_write2_b32 v104, v44, v45 offset1:1
	ds_write2_b32 v105, v50, v51 offset1:1
	ds_write2_b32 v106, v52, v53 offset1:1
	ds_write2_b32 v107, v46, v47 offset1:1
	ds_write2_b32 v108, v48, v49 offset1:1
	ds_write2_b32 v109, v58, v59 offset1:1
	ds_write2_b32 v110, v60, v61 offset1:1
	ds_write2_b32 v111, v54, v55 offset1:1
	ds_write2_b32 v112, v56, v57 offset1:1
	s_waitcnt lgkmcnt(0)
	ds_read2_b32 v[46:47], v101 offset1:8
	ds_read2_b32 v[48:49], v101 offset0:66 offset1:74
	ds_read2_b32 v[52:53], v101 offset0:33 offset1:41
	ds_read2_b32 v[54:55], v101 offset0:99 offset1:107
	ds_read2_b32 v[56:57], v101 offset0:132 offset1:140
	ds_read2_b32 v[58:59], v101 offset0:198 offset1:206
	ds_read2_b32 v[60:61], v101 offset0:165 offset1:173
	ds_read2_b32 v[62:63], v101 offset0:231 offset1:239
	s_ashr_i32 s11, s53, 3
	s_waitcnt lgkmcnt(5)
	v_mov_b32_e32 v44, v52
	s_waitcnt lgkmcnt(4)
	v_mov_b32_e32 v45, v54
	s_waitcnt lgkmcnt(3)
	v_mov_b32_e32 v64, v56
	s_waitcnt lgkmcnt(2)
	v_mov_b32_e32 v65, v58
	s_waitcnt lgkmcnt(1)
	v_mov_b32_e32 v66, v60
	s_waitcnt lgkmcnt(0)
	v_mov_b32_e32 v67, v62
	s_lshr_b32 s16, s51, 6
	v_mov_b32_e32 v42, v46
	v_mov_b32_e32 v43, v48
	v_pk_mul_f32 v[44:45], v[80:81], v[44:45]
	v_pk_mul_f32 v[64:65], v[78:79], v[64:65]
	v_pk_mul_f32 v[66:67], v[96:97], v[66:67]
	s_mul_hi_i32 s17, s11, s16
	s_mul_i32 s11, s11, s16
	s_ashr_i32 s16, s52, 31
	v_pk_mul_f32 v[42:43], v[74:75], v[42:43]
	v_bfe_u32 v46, v67, 16, 1
	v_bfe_u32 v52, v45, 16, 1
	v_bfe_u32 v56, v64, 16, 1
	s_add_u32 s28, s11, s52
	v_bfe_u32 v48, v66, 16, 1
	v_bfe_u32 v54, v44, 16, 1
	v_add3_u32 v52, v45, v52, s97
	v_add3_u32 v45, v67, v46, s97
	v_bfe_u32 v46, v42, 16, 1
	v_add3_u32 v56, v64, v56, s97
	s_addc_u32 s29, s17, s16
	s_and_b32 s10, s10, 0xe0
	v_add3_u32 v54, v44, v54, s97
	v_add3_u32 v44, v66, v48, s97
	v_bfe_u32 v48, v43, 16, 1
	v_bfe_u32 v58, v65, 16, 1
	v_add3_u32 v42, v42, v46, s97
	v_lshrrev_b32_e32 v46, 16, v56
	v_lshl_add_u64 v[50:51], v[92:93], 0, v[94:95]
	v_add3_u32 v58, v65, v58, s97
	v_add3_u32 v43, v43, v48, s97
	v_and_or_b32 v44, v44, s23, v46
	v_or_b32_e32 v46, s10, v87
	s_lshl_b64 s[28:29], s[28:29], 15
	v_lshrrev_b32_e32 v42, 16, v42
	v_lshrrev_b32_e32 v43, 16, v43
	v_lshrrev_b32_e32 v48, 16, v58
	v_lshl_add_u64 v[50:51], v[50:51], 0, s[28:29]
	v_lshlrev_b32_e32 v114, 7, v46
	v_and_or_b32 v45, v45, s23, v48
	v_and_or_b32 v43, v52, s23, v43
	v_and_or_b32 v42, v54, s23, v42
	v_lshl_add_u64 v[64:65], v[50:51], 0, v[114:115]
	v_mov_b32_e32 v48, v47
	v_mov_b32_e32 v54, v53
	v_mov_b32_e32 v62, v61
	global_store_dwordx4 v[64:65], v[42:45], off sc1
	v_mov_b32_e32 v58, v57
	v_pk_mul_f32 v[46:47], v[78:79], v[58:59]
	v_pk_mul_f32 v[42:43], v[74:75], v[48:49]
	v_pk_mul_f32 v[44:45], v[80:81], v[54:55]
	v_pk_mul_f32 v[48:49], v[96:97], v[62:63]
	v_bfe_u32 v54, v45, 16, 1
	v_bfe_u32 v52, v49, 16, 1
	v_add3_u32 v54, v45, v54, s97
	v_add3_u32 v45, v49, v52, s97
	v_bfe_u32 v52, v46, 16, 1
	v_bfe_u32 v53, v48, 16, 1
	v_bfe_u32 v55, v44, 16, 1
	v_add3_u32 v46, v46, v52, s97
	v_add3_u32 v55, v44, v55, s97
	v_add3_u32 v44, v48, v53, s97
	v_bfe_u32 v48, v42, 16, 1
	v_bfe_u32 v49, v43, 16, 1
	v_bfe_u32 v53, v47, 16, 1
	v_lshrrev_b32_e32 v46, 16, v46
	v_add3_u32 v47, v47, v53, s97
	v_add3_u32 v43, v43, v49, s97
	v_add3_u32 v42, v42, v48, s97
	v_and_or_b32 v44, v44, s23, v46
	v_or_b32_e32 v46, s10, v98
	v_lshrrev_b32_e32 v42, 16, v42
	v_lshrrev_b32_e32 v43, 16, v43
	v_lshrrev_b32_e32 v47, 16, v47
	v_lshlrev_b32_e32 v114, 7, v46
	v_and_or_b32 v45, v45, s23, v47
	v_and_or_b32 v43, v54, s23, v43
	v_and_or_b32 v42, v55, s23, v42
	v_lshl_add_u64 v[46:47], v[50:51], 0, v[114:115]
	ds_read2_b32 v[48:49], v101 offset0:16 offset1:24
	ds_read2_b32 v[52:53], v101 offset0:82 offset1:90
	global_store_dwordx4 v[46:47], v[42:45], off sc1
	ds_read2_b32 v[46:47], v101 offset0:49 offset1:57
	ds_read2_b32 v[54:55], v101 offset0:115 offset1:123
	ds_read2_b32 v[56:57], v101 offset0:148 offset1:156
	ds_read2_b32 v[58:59], v101 offset0:214 offset1:222
	ds_read2_b32 v[60:61], v101 offset0:181 offset1:189
	ds_read2_b32 v[62:63], v101 offset0:247 offset1:255
	s_waitcnt lgkmcnt(7)
	v_mov_b32_e32 v42, v48
	s_waitcnt lgkmcnt(5)
	v_mov_b32_e32 v44, v46
	s_waitcnt lgkmcnt(4)
	v_mov_b32_e32 v45, v54
	s_waitcnt lgkmcnt(3)
	v_mov_b32_e32 v64, v56
	s_waitcnt lgkmcnt(2)
	v_mov_b32_e32 v65, v58
	s_waitcnt lgkmcnt(1)
	v_mov_b32_e32 v66, v60
	s_waitcnt lgkmcnt(0)
	v_mov_b32_e32 v67, v62
	v_mov_b32_e32 v43, v52
	v_pk_mul_f32 v[44:45], v[80:81], v[44:45]
	v_pk_mul_f32 v[64:65], v[78:79], v[64:65]
	v_pk_mul_f32 v[66:67], v[96:97], v[66:67]
	v_pk_mul_f32 v[42:43], v[74:75], v[42:43]
	v_bfe_u32 v46, v67, 16, 1
	v_bfe_u32 v52, v45, 16, 1
	v_bfe_u32 v56, v64, 16, 1
	v_bfe_u32 v48, v66, 16, 1
	v_bfe_u32 v54, v44, 16, 1
	v_add3_u32 v52, v45, v52, s97
	v_add3_u32 v45, v67, v46, s97
	v_bfe_u32 v46, v42, 16, 1
	v_add3_u32 v56, v64, v56, s97
	v_add3_u32 v54, v44, v54, s97
	v_add3_u32 v44, v66, v48, s97
	v_bfe_u32 v48, v43, 16, 1
	v_bfe_u32 v58, v65, 16, 1
	v_add3_u32 v42, v42, v46, s97
	v_lshrrev_b32_e32 v46, 16, v56
	v_add3_u32 v58, v65, v58, s97
	v_add3_u32 v43, v43, v48, s97
	v_and_or_b32 v44, v44, s23, v46
	v_or_b32_e32 v46, s10, v99
	v_lshrrev_b32_e32 v42, 16, v42
	v_lshrrev_b32_e32 v43, 16, v43
	v_lshrrev_b32_e32 v48, 16, v58
	v_lshlrev_b32_e32 v114, 7, v46
	v_and_or_b32 v45, v45, s23, v48
	v_and_or_b32 v43, v52, s23, v43
	v_and_or_b32 v42, v54, s23, v42
	v_lshl_add_u64 v[64:65], v[50:51], 0, v[114:115]
	v_mov_b32_e32 v54, v47
	v_mov_b32_e32 v62, v61
	global_store_dwordx4 v[64:65], v[42:45], off sc1
	v_mov_b32_e32 v52, v49
	v_mov_b32_e32 v58, v57
	v_pk_mul_f32 v[44:45], v[80:81], v[54:55]
	v_pk_mul_f32 v[48:49], v[96:97], v[62:63]
	v_pk_mul_f32 v[42:43], v[74:75], v[52:53]
	v_pk_mul_f32 v[46:47], v[78:79], v[58:59]
	v_bfe_u32 v52, v49, 16, 1
	v_bfe_u32 v54, v45, 16, 1
	v_add3_u32 v54, v45, v54, s97
	v_add3_u32 v45, v49, v52, s97
	v_bfe_u32 v52, v46, 16, 1
	v_bfe_u32 v53, v48, 16, 1
	v_bfe_u32 v55, v44, 16, 1
	v_add3_u32 v46, v46, v52, s97
	v_add3_u32 v55, v44, v55, s97
	v_add3_u32 v44, v48, v53, s97
	v_bfe_u32 v48, v42, 16, 1
	v_bfe_u32 v49, v43, 16, 1
	v_bfe_u32 v53, v47, 16, 1
	v_lshrrev_b32_e32 v46, 16, v46
	v_add3_u32 v47, v47, v53, s97
	v_add3_u32 v43, v43, v49, s97
	v_add3_u32 v42, v42, v48, s97
	v_and_or_b32 v44, v44, s23, v46
	v_or_b32_e32 v46, s10, v100
	v_lshrrev_b32_e32 v42, 16, v42
	v_lshrrev_b32_e32 v43, 16, v43
	v_lshrrev_b32_e32 v47, 16, v47
	v_lshlrev_b32_e32 v114, 7, v46
	v_and_or_b32 v45, v45, s23, v47
	v_and_or_b32 v43, v54, s23, v43
	v_and_or_b32 v42, v55, s23, v42
	v_lshl_add_u64 v[46:47], v[50:51], 0, v[114:115]
	global_store_dwordx4 v[46:47], v[42:45], off sc1
	s_waitcnt lgkmcnt(0)
	s_waitcnt vmcnt(13)
	v_cndmask_b32_e64 v5, v5, 1.0, vcc
	v_cndmask_b32_e64 v4, v4, 1.0, vcc
	v_cndmask_b32_e64 v3, v3, 1.0, vcc
	v_cndmask_b32_e64 v2, v2, 1.0, vcc
	s_waitcnt vmcnt(12)
	v_cndmask_b32_e64 v9, v9, 1.0, vcc
	v_cndmask_b32_e64 v8, v8, 1.0, vcc
	v_cndmask_b32_e64 v7, v7, 1.0, vcc
	v_cndmask_b32_e64 v6, v6, 1.0, vcc

.LBB0_914:
	s_sub_i32 s16, s54, s40
	s_and_b64 s[10:11], s[28:29], exec
	s_cselect_b32 s10, s16, 0
	s_lshr_b32 s41, s55, 5
	s_waitcnt vmcnt(10)
	v_cvt_f32_u32_e32 v42, s41
	s_sub_i32 s17, 0, s41
	s_abs_i32 s16, s10
	s_ashr_i32 s11, s10, 31
	v_rcp_iflag_f32_e32 v42, v42
	v_lshlrev_b32_e32 v114, 2, v84
	v_lshlrev_b32_e32 v96, 2, v86
	v_mov_b32_e32 v97, v115
	v_mul_f32_e32 v42, 0x4f7ffffe, v42
	v_cvt_u32_f32_e32 v42, v42
	v_add_u32_e32 v113, 0x420, v102
	v_add_u32_e32 v116, 0x428, v102
	v_add_u32_e32 v117, 0x840, v102
	v_readfirstlane_b32 s38, v42
	s_mul_i32 s17, s17, s38
	s_mul_hi_u32 s17, s38, s17
	s_add_i32 s38, s38, s17
	s_mul_hi_u32 s17, s16, s38
	s_mul_i32 s38, s17, s41
	s_sub_i32 s16, s16, s38
	s_add_i32 s39, s17, 1
	s_sub_i32 s38, s16, s41
	s_cmp_ge_u32 s16, s41
	s_cselect_b32 s17, s39, s17
	s_cselect_b32 s16, s38, s16
	s_add_i32 s38, s17, 1
	s_cmp_ge_u32 s16, s41
	s_cselect_b32 s16, s38, s17
	s_xor_b32 s16, s16, s11
	s_sub_i32 s52, s16, s11
	s_mul_i32 s11, s52, s41
	s_sub_i32 s53, s10, s11
	s_lshl_b32 s38, s52, 6
	s_lshl_b32 s10, s53, 5
	s_waitcnt vmcnt(7)
	v_or_b32_e32 v58, s38, v87
	s_ashr_i32 s11, s10, 31
	s_waitcnt vmcnt(1)
	v_lshl_add_u64 v[42:43], s[10:11], 2, v[82:83]
	s_ashr_i32 s39, s38, 31
	v_or_b32_e32 v44, 8, v58
	v_lshl_add_u64 v[54:55], v[42:43], 0, v[114:115]
	s_mul_i32 s11, s39, s55
	v_mad_u64_u32 v[42:43], s[56:57], v58, s55, 0
	v_mad_u64_u32 v[44:45], s[56:57], v44, s55, 0
	v_add_u32_e32 v43, s11, v43
	v_add_u32_e32 v45, s11, v45
	v_lshl_add_u64 v[42:43], v[42:43], 2, v[54:55]
	v_lshl_add_u64 v[44:45], v[44:45], 2, v[54:55]
	global_load_dwordx4 v[66:69], v[42:43], off nt
	global_load_dwordx4 v[62:65], v[44:45], off nt
	v_or_b32_e32 v42, 16, v58
	v_or_b32_e32 v44, 24, v58
	v_or_b32_e32 v46, 32, v58
	v_or_b32_e32 v48, 40, v58
	v_or_b32_e32 v56, 48, v58
	v_or_b32_e32 v58, 56, v58
	v_mad_u64_u32 v[42:43], s[56:57], v42, s55, 0
	v_mad_u64_u32 v[44:45], s[56:57], v44, s55, 0
	v_mad_u64_u32 v[46:47], s[56:57], v46, s55, 0
	v_mad_u64_u32 v[48:49], s[56:57], v48, s55, 0
	v_mad_u64_u32 v[56:57], s[56:57], v56, s55, 0
	v_mad_u64_u32 v[58:59], s[56:57], v58, s55, 0
	v_add_u32_e32 v43, s11, v43
	v_add_u32_e32 v45, s11, v45
	v_add_u32_e32 v47, s11, v47
	v_add_u32_e32 v49, s11, v49
	v_add_u32_e32 v57, s11, v57
	v_add_u32_e32 v59, s11, v59
	s_lshr_b32 s11, s42, 5
	v_cvt_f32_u32_e32 v76, s11
	s_waitcnt vmcnt(2)
	v_lshl_add_u64 v[74:75], s[38:39], 2, v[88:89]
	v_lshl_add_u64 v[74:75], v[74:75], 0, v[96:97]
	v_cmp_eq_u64_e64 s[38:39], 0, v[88:89]
	v_lshl_add_u64 v[42:43], v[42:43], 2, v[54:55]
	v_lshl_add_u64 v[44:45], v[44:45], 2, v[54:55]
	v_lshl_add_u64 v[46:47], v[46:47], 2, v[54:55]
	v_lshl_add_u64 v[48:49], v[48:49], 2, v[54:55]
	v_lshl_add_u64 v[56:57], v[56:57], 2, v[54:55]
	v_lshl_add_u64 v[54:55], v[58:59], 2, v[54:55]
	v_cndmask_b32_e64 v75, v75, v83, s[38:39]
	v_cndmask_b32_e64 v74, v74, v82, s[38:39]
	global_load_dwordx4 v[70:73], v[42:43], off nt
	s_nop 0
	global_load_dwordx4 v[42:45], v[44:45], off nt
	s_nop 0
	global_load_dwordx4 v[50:53], v[46:47], off nt
	s_nop 0
	global_load_dwordx4 v[46:49], v[48:49], off nt
	s_nop 0
	global_load_dwordx4 v[58:61], v[56:57], off nt
	s_nop 0
	global_load_dwordx4 v[54:57], v[54:55], off nt
	v_rcp_iflag_f32_e32 v94, v76
	global_load_dwordx4 v[78:81], v[74:75], off offset:16
	s_nop 0
	global_load_dwordx4 v[74:77], v[74:75], off
	s_sub_i32 s42, 0, s11
	s_abs_i32 s17, s43
	v_mul_f32_e32 v94, 0x4f7ffffe, v94
	v_cvt_u32_f32_e32 v94, v94
	v_add_u32_e32 v118, 0x848, v102
	v_add_u32_e32 v103, 0xc60, v102
	v_add_u32_e32 v104, 0xc68, v102
	v_readfirstlane_b32 s50, v94
	s_mul_i32 s42, s42, s50
	s_mul_hi_u32 s42, s50, s42
	s_add_i32 s50, s50, s42
	s_mul_hi_u32 s42, s17, s50
	s_mul_i32 s50, s42, s11
	s_sub_i32 s17, s17, s50
	v_add_u32_e32 v105, 0x1080, v102
	v_add_u32_e32 v106, 0x1088, v102
	v_add_u32_e32 v107, 0x14a0, v102
	v_add_u32_e32 v108, 0x14a8, v102
	v_add_u32_e32 v109, 0x18c0, v102
	v_add_u32_e32 v110, 0x18c8, v102
	v_add_u32_e32 v111, 0x1ce0, v102
	v_add_u32_e32 v112, 0x1ce8, v102
	s_ashr_i32 s16, s43, 31
	s_add_i32 s50, s42, 1
	s_sub_i32 s56, s17, s11
	ds_write2_b32 v102, v10, v11 offset1:1
	ds_write2_b32 v102, v12, v13 offset0:2 offset1:3
	ds_write2_b32 v113, v14, v15 offset1:1
	ds_write2_b32 v116, v16, v17 offset1:1
	ds_write2_b32 v117, v18, v19 offset1:1
	ds_write2_b32 v118, v20, v21 offset1:1
	ds_write2_b32 v103, v22, v23 offset1:1
	ds_write2_b32 v104, v24, v25 offset1:1
	ds_write2_b32 v105, v26, v27 offset1:1
	ds_write2_b32 v106, v28, v29 offset1:1
	ds_write2_b32 v107, v30, v31 offset1:1
	ds_write2_b32 v108, v32, v33 offset1:1
	ds_write2_b32 v109, v34, v35 offset1:1
	ds_write2_b32 v110, v36, v37 offset1:1
	ds_write2_b32 v111, v38, v39 offset1:1
	ds_write2_b32 v112, v40, v41 offset1:1
	s_cmp_ge_u32 s17, s11
	s_waitcnt lgkmcnt(0)
	s_cselect_b32 s42, s50, s42
	s_cselect_b32 s17, s56, s17
	s_add_i32 s50, s42, 1
	ds_read2_b32 v[16:17], v101 offset0:33 offset1:41
	ds_read2_b32 v[18:19], v101 offset1:8
	ds_read2_b32 v[20:21], v101 offset0:66 offset1:74
	ds_read2_b32 v[22:23], v101 offset0:99 offset1:107
	ds_read2_b32 v[26:27], v101 offset0:132 offset1:140
	ds_read2_b32 v[28:29], v101 offset0:165 offset1:173
	ds_read2_b32 v[30:31], v101 offset0:198 offset1:206
	ds_read2_b32 v[32:33], v101 offset0:231 offset1:239
	s_cmp_ge_u32 s17, s11
	s_cselect_b32 s17, s50, s42
	s_xor_b32 s17, s17, s16
	s_sub_i32 s16, s17, s16
	s_mul_i32 s11, s16, s11
	v_mov_b32_e32 v34, v6
	v_mov_b32_e32 v35, v8
	v_mov_b32_e32 v8, v7
	s_waitcnt lgkmcnt(2)
	v_mov_b32_e32 v6, v28
	s_waitcnt lgkmcnt(0)
	v_mov_b32_e32 v7, v32
	s_sub_i32 s11, s43, s11
	v_mov_b32_e32 v24, v2
	v_mov_b32_e32 v25, v4
	v_mov_b32_e32 v10, v18
	v_mov_b32_e32 v11, v20
	v_mov_b32_e32 v4, v3
	v_mov_b32_e32 v2, v16
	v_mov_b32_e32 v3, v22
	v_pk_mul_f32 v[6:7], v[8:9], v[6:7]
	s_lshl_b32 s17, s11, 5
	s_ashr_i32 s11, s11, 3
	s_lshr_b32 s14, s14, 6
	v_pk_mul_f32 v[10:11], v[24:25], v[10:11]
	v_pk_mul_f32 v[2:3], v[4:5], v[2:3]
	v_mov_b32_e32 v12, v26
	v_mov_b32_e32 v13, v30
	v_bfe_u32 v16, v7, 16, 1
	s_mul_hi_i32 s43, s11, s14
	s_mul_i32 s11, s11, s14
	s_ashr_i32 s14, s16, 31
	v_pk_mul_f32 v[12:13], v[34:35], v[12:13]
	v_bfe_u32 v18, v6, 16, 1
	v_bfe_u32 v20, v3, 16, 1
	v_bfe_u32 v22, v2, 16, 1
	v_add3_u32 v7, v7, v16, s97
	v_bfe_u32 v16, v10, 16, 1
	s_add_u32 s42, s11, s16
	v_add3_u32 v2, v2, v22, s97
	v_add3_u32 v3, v3, v20, s97
	v_add3_u32 v6, v6, v18, s97
	v_bfe_u32 v18, v11, 16, 1
	v_bfe_u32 v20, v12, 16, 1
	v_bfe_u32 v22, v13, 16, 1
	v_add3_u32 v10, v10, v16, s97
	s_addc_u32 s43, s43, s14
	s_and_b32 s11, s17, 0xe0
	v_lshlrev_b32_e32 v94, 1, v86
	v_mov_b32_e32 v95, v115
	v_add3_u32 v13, v13, v22, s97
	v_add3_u32 v12, v12, v20, s97
	v_add3_u32 v11, v11, v18, s97
	v_lshrrev_b32_e32 v10, 16, v10
	v_lshl_add_u64 v[14:15], v[90:91], 0, v[94:95]
	v_lshrrev_b32_e32 v11, 16, v11
	v_lshrrev_b32_e32 v12, 16, v12
	v_lshrrev_b32_e32 v13, 16, v13
	v_and_or_b32 v10, v2, s23, v10
	v_or_b32_e32 v2, s11, v87
	s_lshl_b64 s[42:43], s[42:43], 15
	v_and_or_b32 v13, v7, s23, v13
	v_and_or_b32 v12, v6, s23, v12
	v_and_or_b32 v11, v3, s23, v11
	v_lshl_add_u64 v[6:7], v[14:15], 0, s[42:43]
	v_lshlrev_b32_e32 v2, 7, v2
	v_mov_b32_e32 v3, v115
	v_mov_b32_e32 v32, v29
	v_lshl_add_u64 v[2:3], v[6:7], 0, v[2:3]
	v_mov_b32_e32 v20, v19
	v_pk_mul_f32 v[14:15], v[8:9], v[32:33]
	global_store_dwordx4 v[2:3], v[10:13], off sc1
	v_pk_mul_f32 v[2:3], v[24:25], v[20:21]
	v_mov_b32_e32 v22, v17
	v_bfe_u32 v16, v15, 16, 1
	v_pk_mul_f32 v[10:11], v[4:5], v[22:23]
	v_mov_b32_e32 v30, v27
	v_bfe_u32 v17, v14, 16, 1
	v_add3_u32 v15, v15, v16, s97
	v_bfe_u32 v16, v2, 16, 1
	v_pk_mul_f32 v[12:13], v[34:35], v[30:31]
	v_bfe_u32 v18, v11, 16, 1
	v_bfe_u32 v19, v10, 16, 1
	v_add3_u32 v14, v14, v17, s97
	v_bfe_u32 v17, v3, 16, 1
	v_add3_u32 v2, v2, v16, s97
	v_add3_u32 v10, v10, v19, s97
	v_add3_u32 v11, v11, v18, s97
	v_bfe_u32 v18, v12, 16, 1
	v_bfe_u32 v19, v13, 16, 1
	v_add3_u32 v3, v3, v17, s97
	v_lshrrev_b32_e32 v2, 16, v2
	v_add3_u32 v13, v13, v19, s97
	v_add3_u32 v12, v12, v18, s97
	v_lshrrev_b32_e32 v3, 16, v3
	v_and_or_b32 v10, v10, s23, v2
	v_or_b32_e32 v2, s11, v98
	v_lshrrev_b32_e32 v12, 16, v12
	v_lshrrev_b32_e32 v13, 16, v13
	v_and_or_b32 v11, v11, s23, v3
	v_lshlrev_b32_e32 v2, 7, v2
	v_mov_b32_e32 v3, v115
	v_and_or_b32 v13, v15, s23, v13
	v_and_or_b32 v12, v14, s23, v12
	v_lshl_add_u64 v[2:3], v[6:7], 0, v[2:3]
	ds_read2_b32 v[14:15], v101 offset0:16 offset1:24
	ds_read2_b32 v[16:17], v101 offset0:82 offset1:90
	global_store_dwordx4 v[2:3], v[10:13], off sc1
	ds_read2_b32 v[2:3], v101 offset0:49 offset1:57
	ds_read2_b32 v[18:19], v101 offset0:115 offset1:123
	ds_read2_b32 v[20:21], v101 offset0:148 offset1:156
	ds_read2_b32 v[22:23], v101 offset0:214 offset1:222
	ds_read2_b32 v[26:27], v101 offset0:181 offset1:189
	ds_read2_b32 v[28:29], v101 offset0:247 offset1:255
	s_waitcnt lgkmcnt(7)
	v_mov_b32_e32 v10, v14
	s_waitcnt lgkmcnt(5)
	v_mov_b32_e32 v12, v2
	s_waitcnt lgkmcnt(4)
	v_mov_b32_e32 v13, v18
	v_mov_b32_e32 v11, v16
	v_pk_mul_f32 v[12:13], v[4:5], v[12:13]
	s_waitcnt lgkmcnt(3)
	v_mov_b32_e32 v30, v20
	s_waitcnt lgkmcnt(2)
	v_mov_b32_e32 v31, v22
	v_pk_mul_f32 v[10:11], v[24:25], v[10:11]
	v_pk_mul_f32 v[30:31], v[34:35], v[30:31]
	s_waitcnt lgkmcnt(1)
	v_mov_b32_e32 v32, v26
	s_waitcnt lgkmcnt(0)
	v_mov_b32_e32 v33, v28
	v_bfe_u32 v16, v13, 16, 1
	v_pk_mul_f32 v[32:33], v[8:9], v[32:33]
	v_add3_u32 v16, v13, v16, s97
	v_bfe_u32 v13, v10, 16, 1
	v_bfe_u32 v22, v31, 16, 1
	v_bfe_u32 v2, v33, 16, 1
	v_bfe_u32 v18, v12, 16, 1
	v_add3_u32 v22, v31, v22, s97
	v_add3_u32 v10, v10, v13, s97
	v_bfe_u32 v14, v32, 16, 1
	v_add3_u32 v18, v12, v18, s97
	v_add3_u32 v2, v33, v2, s97
	v_bfe_u32 v20, v30, 16, 1
	v_lshrrev_b32_e32 v10, 16, v10
	v_lshrrev_b32_e32 v13, 16, v22
	v_add3_u32 v12, v32, v14, s97
	v_bfe_u32 v14, v11, 16, 1
	v_add3_u32 v20, v30, v20, s97
	v_and_or_b32 v13, v2, s23, v13
	v_and_or_b32 v10, v18, s23, v10
	v_or_b32_e32 v2, s11, v99
	v_mov_b32_e32 v18, v3
	v_add3_u32 v11, v11, v14, s97
	v_lshrrev_b32_e32 v14, 16, v20
	v_lshlrev_b32_e32 v30, 7, v2
	v_pk_mul_f32 v[2:3], v[4:5], v[18:19]
	v_mov_b32_e32 v22, v21
	v_lshrrev_b32_e32 v11, 16, v11
	v_and_or_b32 v12, v12, s23, v14
	v_mov_b32_e32 v31, v115
	v_pk_mul_f32 v[4:5], v[34:35], v[22:23]
	v_mov_b32_e32 v28, v27
	v_bfe_u32 v14, v3, 16, 1
	v_and_or_b32 v11, v16, s23, v11
	v_lshl_add_u64 v[30:31], v[6:7], 0, v[30:31]
	v_mov_b32_e32 v16, v15
	v_pk_mul_f32 v[8:9], v[8:9], v[28:29]
	v_bfe_u32 v15, v2, 16, 1
	v_add3_u32 v3, v3, v14, s97
	v_bfe_u32 v14, v4, 16, 1
	global_store_dwordx4 v[30:31], v[10:13], off sc1
	v_add3_u32 v2, v2, v15, s97
	v_bfe_u32 v15, v5, 16, 1
	v_pk_mul_f32 v[10:11], v[24:25], v[16:17]
	v_bfe_u32 v12, v9, 16, 1
	v_bfe_u32 v13, v8, 16, 1
	v_add3_u32 v4, v4, v14, s97
	v_add3_u32 v8, v8, v13, s97
	v_add3_u32 v9, v9, v12, s97
	v_bfe_u32 v12, v10, 16, 1
	v_bfe_u32 v13, v11, 16, 1
	v_add3_u32 v5, v5, v15, s97
	v_lshrrev_b32_e32 v4, 16, v4
	v_add3_u32 v11, v11, v13, s97
	v_add3_u32 v10, v10, v12, s97
	v_lshrrev_b32_e32 v5, 16, v5
	v_and_or_b32 v4, v8, s23, v4
	v_or_b32_e32 v8, s11, v100
	v_lshrrev_b32_e32 v10, 16, v10
	v_lshrrev_b32_e32 v11, 16, v11
	v_and_or_b32 v5, v9, s23, v5
	v_lshlrev_b32_e32 v8, 7, v8
	v_mov_b32_e32 v9, v115
	v_and_or_b32 v3, v3, s23, v11
	v_and_or_b32 v2, v2, s23, v10
	v_lshl_add_u64 v[6:7], v[6:7], 0, v[8:9]
	global_store_dwordx4 v[6:7], v[2:5], off sc1
	s_waitcnt lgkmcnt(0)
	s_andn2_b64 vcc, exec, s[28:29]
	s_cbranch_vccnz .LBB0_844
	s_add_i32 s50, s54, s60
	s_add_i32 s11, s40, s24
	s_cmp_lt_i32 s50, s11
	s_mov_b64 s[28:29], -1
	s_cbranch_scc1 .LBB0_842
	s_add_i32 s56, s15, 1
	s_max_i32 s54, s20, s56
	s_cmp_ge_i32 s56, s20
	s_mov_b64 s[28:29], 0
	s_cbranch_scc1 .LBB0_981
	s_add_i32 s57, s15, 1
	s_cmp_lt_i32 s15, 3
	s_cbranch_scc1 .LBB0_950
